# speedup vs baseline: 1.0063x; 1.0063x over previous
_Z9l1_kernelPKiS0_P15HIP_vector_typeIjLj2EEPiS4_PKfS6_S6_S6_PfP6__half:
	s_cmp_gt_u32 s2, 42
	s_mov_b64 s[4:5], -1
	s_cbranch_scc0 .LBB0_17
	s_mul_i32 s15, s2, 0xeb
	s_add_i32 s3, s15, 0xffffd887
	s_min_i32 s16, s3, 0xc265
	s_add_i32 s12, s16, 0xeb
	s_cmp_ge_i32 s3, s12
	s_cbranch_scc1 .LBB0_16
	s_load_dwordx4 s[4:7], s[0:1], 0x28
	s_load_dwordx2 s[10:11], s[0:1], 0x38
	s_load_dwordx4 s[24:27], s[0:1], 0x40
	s_load_dwordx2 s[28:29], s[0:1], 0x50
	v_lshlrev_b32_e32 v1, 4, v0
	v_and_b32_e32 v2, 0x1f0, v1
	v_mov_b32_e32 v3, 0
	v_lshrrev_b32_e32 v1, 5, v0
	s_add_i32 s13, s16, 0xea
	s_waitcnt lgkmcnt(0)
	v_lshl_add_u64 v[110:111], s[4:5], 0, v[2:3]
	v_add_u32_e32 v2, s3, v1
	v_min_i32_e32 v2, s13, v2
	v_ashrrev_i32_e32 v3, 31, v2
	v_lshlrev_b64 v[2:3], 9, v[2:3]
	v_lshl_add_u64 v[10:11], v[110:111], 0, v[2:3]
	v_or_b32_e32 v2, 0x200, v0
	v_lshrrev_b32_e32 v146, 5, v2
	v_add_u32_e32 v2, s3, v146
	v_min_i32_e32 v2, s13, v2
	v_ashrrev_i32_e32 v3, 31, v2
	v_lshlrev_b64 v[2:3], 9, v[2:3]
	v_or_b32_e32 v147, 32, v1
	v_lshl_add_u64 v[12:13], v[110:111], 0, v[2:3]
	global_load_dwordx4 v[2:5], v[10:11], off
	global_load_dwordx4 v[6:9], v[12:13], off
	v_add_u32_e32 v10, s3, v147
	v_min_i32_e32 v10, s13, v10
	v_ashrrev_i32_e32 v11, 31, v10
	v_lshlrev_b64 v[10:11], 9, v[10:11]
	v_lshl_add_u64 v[10:11], v[110:111], 0, v[10:11]
	global_load_dwordx4 v[10:13], v[10:11], off
	v_lshrrev_b32_e32 v149, 6, v0
	s_movk_i32 s4, 0x200
	v_and_b32_e32 v150, 15, v0
	v_cmp_gt_u32_e32 vcc, s4, v0
	v_lshlrev_b32_e32 v151, 4, v149
	s_and_saveexec_b64 s[4:5], vcc
	s_xor_b64 s[4:5], exec, s[4:5]
	v_or_b32_e32 v32, v151, v150
	s_or_saveexec_b64 s[4:5], s[4:5]
	v_lshlrev_b32_e32 v14, 1, v150
	v_mov_b64_e32 v[30:31], s[6:7]
	s_xor_b64 exec, exec, s[4:5]
	v_and_b32_e32 v15, 0x60, v151
	v_bfe_u32 v16, v0, 6, 1
	v_or3_b32 v32, v16, v15, v14
	v_mov_b64_e32 v[30:31], s[10:11]
	s_or_b64 exec, exec, s[4:5]
	s_movk_i32 s17, 0x110
	s_mov_b32 s14, 0x7060302
	s_sub_i32 s19, s16, s3
	s_addk_i32 s19, 0x11a
	v_readfirstlane_b32 s30, v149
	v_bfe_u32 v152, v0, 4, 2
	v_lshlrev_b32_e32 v153, 5, v149
	v_and_b32_e32 v153, 0x60, v153
	v_or_b32_e32 v144, v151, v150
	v_lshlrev_b32_e32 v144, 2, v144
	v_lshl_add_u32 v144, v152, 12, v144
	v_lshlrev_b32_e32 v145, 3, v150
	v_lshl_add_u32 v145, v153, 2, v145
	v_lshl_add_u32 v145, v152, 12, v145
	s_waitcnt lgkmcnt(0)
	s_cmp_lt_u32 s30, 4
	s_cselect_b32 s20, s10, s24
	s_cselect_b32 s21, s11, s25
	s_cbranch_scc1 .Lg_prio_done
	s_setprio 1
.Lg_prio_done:
	s_add_u32 s32, s6, 0x4000
	s_addc_u32 s33, s7, 0
	s_add_u32 s34, s6, 0x8000
	s_addc_u32 s35, s7, 0
	s_add_u32 s36, s6, 0xc000
	s_addc_u32 s37, s7, 0
	s_add_u32 s38, s20, 0x4000
	s_addc_u32 s39, s21, 0
	s_add_u32 s40, s20, 0x8000
	s_addc_u32 s41, s21, 0
	s_add_u32 s42, s20, 0xc000
	s_addc_u32 s43, s21, 0
	s_mul_hi_u32 s5, s19, 0xaaaaaaab
	s_addk_i32 s16, 0xfa
	s_lshr_b32 s10, s5, 5
	s_mov_b32 s11, 0
	s_add_i32 s31, s30, s2
	s_and_b32 s31, s31, 7
	s_cmp_eq_u32 s31, 1
	s_cbranch_scc1 .Lw_rot_1
	s_cmp_eq_u32 s31, 2
	s_cbranch_scc1 .Lw_rot_2
	s_cmp_eq_u32 s31, 3
	s_cbranch_scc1 .Lw_rot_3
	s_cmp_eq_u32 s31, 4
	s_cbranch_scc1 .Lw_rot_4
	s_cmp_eq_u32 s31, 5
	s_cbranch_scc1 .Lw_rot_5
	s_cmp_eq_u32 s31, 6
	s_cbranch_scc1 .Lw_rot_6
	s_cmp_eq_u32 s31, 7
	s_cbranch_scc1 .Lw_rot_7
